# down-weight conversion prologue: four row-scale loads issued together (on top of the MoE unit table)
# baseline (speedup 1.0000x reference)
; #define LAS __attribute__((address_space(3)))
; __device__ __forceinline__ ConvItem conv_item(const Params& p, int it) {
;     constexpr int I_E = (DM / 128) * (DFF / 64);
;     const bool dn = it >= NEXP * 2 * I_E; const int j = dn ? it - NEXP * 2 * I_E : it;
;     const int e = dn ? j / I_E : j / (2 * I_E), which = dn ? 2 : (j % (2 * I_E)) / I_E, r3 = j % I_E, nb = r3 % (DFF / 64), kb = r3 / (DFF / 64), n0 = nb * 64;
; __device__ __forceinline__ void moe_weight_convert(const Params& p, Frame& F, int gw, int NGW, int it0, int NIT) {
;     ...
;     for (int i = F.tid; i < DM; i += 512) { *(LAS float*)(F.lds + 4 * i) = p.in[11][i] * 64.0f; *(LAS float*)(F.lds + 8192 + 4 * i) = 64.0f; }
;     __syncthreads();
;     int it = it0 + gw; if (it >= NIT) return;
;     ConvItem cur = conv_item(p, it);
.LBB0_877:
	global_load_dword v6, v[2:3], off
	global_load_dword v240, v[2:3], off offset:2048
	v_lshl_add_u64 v[246:247], v[2:3], 0, s[2:3]
	s_nop 0
	v_lshl_add_u64 v[246:247], v[246:247], 0, s[2:3]
	global_load_dword v241, v[246:247], off
	global_load_dword v242, v[246:247], off offset:2048
	s_waitcnt vmcnt(0)
	v_mul_f32_e32 v6, 0x42800000, v6
	v_mul_f32_e32 v240, 0x42800000, v240
	v_mul_f32_e32 v241, 0x42800000, v241
	v_mul_f32_e32 v242, 0x42800000, v242
	ds_write2st64_b32 v4, v6, v5 offset1:32
	v_add_u32_e32 v4, 0x800, v4
	ds_write2st64_b32 v4, v240, v5 offset1:32
	v_add_u32_e32 v4, 0x800, v4
	ds_write2st64_b32 v4, v241, v5 offset1:32
	v_add_u32_e32 v4, 0x800, v4
	ds_write2st64_b32 v4, v242, v5 offset1:32
	v_add_u32_e32 v4, 0x800, v4
	s_or_b64 exec, exec, s[0:1]
	v_readlane_b32 s0, v245, 18
	s_sub_i32 s0, s0, s34
	s_lshl_b32 s7, s0, 3
	s_add_i32 s7, s7, s54
	s_cmpk_lt_i32 s7, 0x4000
	s_waitcnt lgkmcnt(0)
	s_barrier
	s_cbranch_scc0 .LBB0_914
	s_add_i32 s8, s7, 0x8000
	s_cmp_gt_i32 s7, -1
	s_cselect_b64 s[0:1], -1, 0
	s_cmp_lt_i32 s7, 0
	s_cselect_b64 s[2:3], -1, 0
	s_and_b64 vcc, exec, s[2:3]
	s_cbranch_vccz .LBB0_882
	s_ashr_i32 s4, s8, 31
	s_lshr_b32 s4, s4, 22
	s_add_i32 s4, s8, s4
	s_ashr_i32 s6, s4, 10
	s_cbranch_execz .LBB0_883
	s_branch .LBB0_884
